# phase prologues: forget-weight and sub-key staging loops issue their loads in batches of 16 instead of one round trip per piece (on top of v5)
# speedup vs baseline: 1.0239x; 1.0115x over previous
.LBB0_228:
	s_mov_b64 s[98:99], 0x2000
	v_ashrrev_i32_e32 v5, 31, v4
	v_lshl_add_u64 v[140:141], v[4:5], 2, s[12:13]
	global_load_dwordx4 v[144:147], v[140:141], off
	v_lshl_add_u64 v[140:141], v[140:141], 0, s[98:99]
	global_load_dwordx4 v[148:151], v[140:141], off
	v_lshl_add_u64 v[140:141], v[140:141], 0, s[98:99]
	global_load_dwordx4 v[152:155], v[140:141], off
	v_lshl_add_u64 v[140:141], v[140:141], 0, s[98:99]
	global_load_dwordx4 v[156:159], v[140:141], off
	v_lshl_add_u64 v[140:141], v[140:141], 0, s[98:99]
	global_load_dwordx4 v[160:163], v[140:141], off
	v_lshl_add_u64 v[140:141], v[140:141], 0, s[98:99]
	global_load_dwordx4 v[164:167], v[140:141], off
	v_lshl_add_u64 v[140:141], v[140:141], 0, s[98:99]
	global_load_dwordx4 v[168:171], v[140:141], off
	v_lshl_add_u64 v[140:141], v[140:141], 0, s[98:99]
	global_load_dwordx4 v[172:175], v[140:141], off
	v_lshl_add_u64 v[140:141], v[140:141], 0, s[98:99]
	global_load_dwordx4 v[176:179], v[140:141], off
	v_lshl_add_u64 v[140:141], v[140:141], 0, s[98:99]
	global_load_dwordx4 v[180:183], v[140:141], off
	v_lshl_add_u64 v[140:141], v[140:141], 0, s[98:99]
	global_load_dwordx4 v[184:187], v[140:141], off
	v_lshl_add_u64 v[140:141], v[140:141], 0, s[98:99]
	global_load_dwordx4 v[188:191], v[140:141], off
	v_lshl_add_u64 v[140:141], v[140:141], 0, s[98:99]
	global_load_dwordx4 v[192:195], v[140:141], off
	v_lshl_add_u64 v[140:141], v[140:141], 0, s[98:99]
	global_load_dwordx4 v[196:199], v[140:141], off
	v_lshl_add_u64 v[140:141], v[140:141], 0, s[98:99]
	global_load_dwordx4 v[200:203], v[140:141], off
	v_lshl_add_u64 v[140:141], v[140:141], 0, s[98:99]
	global_load_dwordx4 v[204:207], v[140:141], off
	v_lshl_add_u64 v[140:141], v[140:141], 0, s[98:99]
	s_waitcnt vmcnt(15)
	v_bfe_u32 v5, v144, 16, 1
	v_bfe_u32 v10, v145, 16, 1
	v_bfe_u32 v11, v146, 16, 1
	v_bfe_u32 v12, v147, 16, 1
	v_add3_u32 v5, v144, v5, s3
	v_add3_u32 v6, v145, v10, s3
	v_add3_u32 v7, v146, v11, s3
	v_add3_u32 v12, v147, v12, s3
	v_lshrrev_b32_e32 v5, 16, v5
	v_lshrrev_b32_e32 v7, 16, v7
	v_and_or_b32 v6, v6, s18, v5
	v_and_or_b32 v7, v12, s18, v7
	ds_write_b64 v3, v[6:7]
	s_waitcnt vmcnt(14)
	v_bfe_u32 v5, v148, 16, 1
	v_bfe_u32 v10, v149, 16, 1
	v_bfe_u32 v11, v150, 16, 1
	v_bfe_u32 v12, v151, 16, 1
	v_add3_u32 v5, v148, v5, s3
	v_add3_u32 v6, v149, v10, s3
	v_add3_u32 v7, v150, v11, s3
	v_add3_u32 v12, v151, v12, s3
	v_lshrrev_b32_e32 v5, 16, v5
	v_lshrrev_b32_e32 v7, 16, v7
	v_and_or_b32 v6, v6, s18, v5
	v_and_or_b32 v7, v12, s18, v7
	ds_write_b64 v3, v[6:7] offset:4096
	s_waitcnt vmcnt(13)
	v_bfe_u32 v5, v152, 16, 1
	v_bfe_u32 v10, v153, 16, 1
	v_bfe_u32 v11, v154, 16, 1
	v_bfe_u32 v12, v155, 16, 1
	v_add3_u32 v5, v152, v5, s3
	v_add3_u32 v6, v153, v10, s3
	v_add3_u32 v7, v154, v11, s3
	v_add3_u32 v12, v155, v12, s3
	v_lshrrev_b32_e32 v5, 16, v5
	v_lshrrev_b32_e32 v7, 16, v7
	v_and_or_b32 v6, v6, s18, v5
	v_and_or_b32 v7, v12, s18, v7
	ds_write_b64 v3, v[6:7] offset:8192
	s_waitcnt vmcnt(12)
	v_bfe_u32 v5, v156, 16, 1
	v_bfe_u32 v10, v157, 16, 1
	v_bfe_u32 v11, v158, 16, 1
	v_bfe_u32 v12, v159, 16, 1
	v_add3_u32 v5, v156, v5, s3
	v_add3_u32 v6, v157, v10, s3
	v_add3_u32 v7, v158, v11, s3
	v_add3_u32 v12, v159, v12, s3
	v_lshrrev_b32_e32 v5, 16, v5
	v_lshrrev_b32_e32 v7, 16, v7
	v_and_or_b32 v6, v6, s18, v5
	v_and_or_b32 v7, v12, s18, v7
	ds_write_b64 v3, v[6:7] offset:12288
	s_waitcnt vmcnt(11)
	v_bfe_u32 v5, v160, 16, 1
	v_bfe_u32 v10, v161, 16, 1
	v_bfe_u32 v11, v162, 16, 1
	v_bfe_u32 v12, v163, 16, 1
	v_add3_u32 v5, v160, v5, s3
	v_add3_u32 v6, v161, v10, s3
	v_add3_u32 v7, v162, v11, s3
	v_add3_u32 v12, v163, v12, s3
	v_lshrrev_b32_e32 v5, 16, v5
	v_lshrrev_b32_e32 v7, 16, v7
	v_and_or_b32 v6, v6, s18, v5
	v_and_or_b32 v7, v12, s18, v7
	ds_write_b64 v3, v[6:7] offset:16384
	s_waitcnt vmcnt(10)
	v_bfe_u32 v5, v164, 16, 1
	v_bfe_u32 v10, v165, 16, 1
	v_bfe_u32 v11, v166, 16, 1
	v_bfe_u32 v12, v167, 16, 1
	v_add3_u32 v5, v164, v5, s3
	v_add3_u32 v6, v165, v10, s3
	v_add3_u32 v7, v166, v11, s3
	v_add3_u32 v12, v167, v12, s3
	v_lshrrev_b32_e32 v5, 16, v5
	v_lshrrev_b32_e32 v7, 16, v7
	v_and_or_b32 v6, v6, s18, v5
	v_and_or_b32 v7, v12, s18, v7
	ds_write_b64 v3, v[6:7] offset:20480
	s_waitcnt vmcnt(9)
	v_bfe_u32 v5, v168, 16, 1
	v_bfe_u32 v10, v169, 16, 1
	v_bfe_u32 v11, v170, 16, 1
	v_bfe_u32 v12, v171, 16, 1
	v_add3_u32 v5, v168, v5, s3
	v_add3_u32 v6, v169, v10, s3
	v_add3_u32 v7, v170, v11, s3
	v_add3_u32 v12, v171, v12, s3
	v_lshrrev_b32_e32 v5, 16, v5
	v_lshrrev_b32_e32 v7, 16, v7
	v_and_or_b32 v6, v6, s18, v5
	v_and_or_b32 v7, v12, s18, v7
	ds_write_b64 v3, v[6:7] offset:24576
	s_waitcnt vmcnt(8)
	v_bfe_u32 v5, v172, 16, 1
	v_bfe_u32 v10, v173, 16, 1
	v_bfe_u32 v11, v174, 16, 1
	v_bfe_u32 v12, v175, 16, 1
	v_add3_u32 v5, v172, v5, s3
	v_add3_u32 v6, v173, v10, s3
	v_add3_u32 v7, v174, v11, s3
	v_add3_u32 v12, v175, v12, s3
	v_lshrrev_b32_e32 v5, 16, v5
	v_lshrrev_b32_e32 v7, 16, v7
	v_and_or_b32 v6, v6, s18, v5
	v_and_or_b32 v7, v12, s18, v7
	ds_write_b64 v3, v[6:7] offset:28672
	s_waitcnt vmcnt(7)
	v_bfe_u32 v5, v176, 16, 1
	v_bfe_u32 v10, v177, 16, 1
	v_bfe_u32 v11, v178, 16, 1
	v_bfe_u32 v12, v179, 16, 1
	v_add3_u32 v5, v176, v5, s3
	v_add3_u32 v6, v177, v10, s3
	v_add3_u32 v7, v178, v11, s3
	v_add3_u32 v12, v179, v12, s3
	v_lshrrev_b32_e32 v5, 16, v5
	v_lshrrev_b32_e32 v7, 16, v7
	v_and_or_b32 v6, v6, s18, v5
	v_and_or_b32 v7, v12, s18, v7
	ds_write_b64 v3, v[6:7] offset:32768
	s_waitcnt vmcnt(6)
	v_bfe_u32 v5, v180, 16, 1
	v_bfe_u32 v10, v181, 16, 1
	v_bfe_u32 v11, v182, 16, 1
	v_bfe_u32 v12, v183, 16, 1
	v_add3_u32 v5, v180, v5, s3
	v_add3_u32 v6, v181, v10, s3
	v_add3_u32 v7, v182, v11, s3
	v_add3_u32 v12, v183, v12, s3
	v_lshrrev_b32_e32 v5, 16, v5
	v_lshrrev_b32_e32 v7, 16, v7
	v_and_or_b32 v6, v6, s18, v5
	v_and_or_b32 v7, v12, s18, v7
	ds_write_b64 v3, v[6:7] offset:36864
	s_waitcnt vmcnt(5)
	v_bfe_u32 v5, v184, 16, 1
	v_bfe_u32 v10, v185, 16, 1
	v_bfe_u32 v11, v186, 16, 1
	v_bfe_u32 v12, v187, 16, 1
	v_add3_u32 v5, v184, v5, s3
	v_add3_u32 v6, v185, v10, s3
	v_add3_u32 v7, v186, v11, s3
	v_add3_u32 v12, v187, v12, s3
	v_lshrrev_b32_e32 v5, 16, v5
	v_lshrrev_b32_e32 v7, 16, v7
	v_and_or_b32 v6, v6, s18, v5
	v_and_or_b32 v7, v12, s18, v7
	ds_write_b64 v3, v[6:7] offset:40960
	s_waitcnt vmcnt(4)
	v_bfe_u32 v5, v188, 16, 1
	v_bfe_u32 v10, v189, 16, 1
	v_bfe_u32 v11, v190, 16, 1
	v_bfe_u32 v12, v191, 16, 1
	v_add3_u32 v5, v188, v5, s3
	v_add3_u32 v6, v189, v10, s3
	v_add3_u32 v7, v190, v11, s3
	v_add3_u32 v12, v191, v12, s3
	v_lshrrev_b32_e32 v5, 16, v5
	v_lshrrev_b32_e32 v7, 16, v7
	v_and_or_b32 v6, v6, s18, v5
	v_and_or_b32 v7, v12, s18, v7
	ds_write_b64 v3, v[6:7] offset:45056
	s_waitcnt vmcnt(3)
	v_bfe_u32 v5, v192, 16, 1
	v_bfe_u32 v10, v193, 16, 1
	v_bfe_u32 v11, v194, 16, 1
	v_bfe_u32 v12, v195, 16, 1
	v_add3_u32 v5, v192, v5, s3
	v_add3_u32 v6, v193, v10, s3
	v_add3_u32 v7, v194, v11, s3
	v_add3_u32 v12, v195, v12, s3
	v_lshrrev_b32_e32 v5, 16, v5
	v_lshrrev_b32_e32 v7, 16, v7
	v_and_or_b32 v6, v6, s18, v5
	v_and_or_b32 v7, v12, s18, v7
	ds_write_b64 v3, v[6:7] offset:49152
	s_waitcnt vmcnt(2)
	v_bfe_u32 v5, v196, 16, 1
	v_bfe_u32 v10, v197, 16, 1
	v_bfe_u32 v11, v198, 16, 1
	v_bfe_u32 v12, v199, 16, 1
	v_add3_u32 v5, v196, v5, s3
	v_add3_u32 v6, v197, v10, s3
	v_add3_u32 v7, v198, v11, s3
	v_add3_u32 v12, v199, v12, s3
	v_lshrrev_b32_e32 v5, 16, v5
	v_lshrrev_b32_e32 v7, 16, v7
	v_and_or_b32 v6, v6, s18, v5
	v_and_or_b32 v7, v12, s18, v7
	ds_write_b64 v3, v[6:7] offset:53248
	s_waitcnt vmcnt(1)
	v_bfe_u32 v5, v200, 16, 1
	v_bfe_u32 v10, v201, 16, 1
	v_bfe_u32 v11, v202, 16, 1
	v_bfe_u32 v12, v203, 16, 1
	v_add3_u32 v5, v200, v5, s3
	v_add3_u32 v6, v201, v10, s3
	v_add3_u32 v7, v202, v11, s3
	v_add3_u32 v12, v203, v12, s3
	v_lshrrev_b32_e32 v5, 16, v5
	v_lshrrev_b32_e32 v7, 16, v7
	v_and_or_b32 v6, v6, s18, v5
	v_and_or_b32 v7, v12, s18, v7
	ds_write_b64 v3, v[6:7] offset:57344
	s_waitcnt vmcnt(0)
	v_bfe_u32 v5, v204, 16, 1
	v_bfe_u32 v10, v205, 16, 1
	v_bfe_u32 v11, v206, 16, 1
	v_bfe_u32 v12, v207, 16, 1
	v_add3_u32 v5, v204, v5, s3
	v_add3_u32 v6, v205, v10, s3
	v_add3_u32 v7, v206, v11, s3
	v_add3_u32 v12, v207, v12, s3
	v_lshrrev_b32_e32 v5, 16, v5
	v_lshrrev_b32_e32 v7, 16, v7
	v_and_or_b32 v6, v6, s18, v5
	v_and_or_b32 v7, v12, s18, v7
	ds_write_b64 v3, v[6:7] offset:61440
	v_add_u32_e32 v3, 0x10000, v3
	global_load_dwordx4 v[144:147], v[140:141], off
	v_lshl_add_u64 v[140:141], v[140:141], 0, s[98:99]
	global_load_dwordx4 v[148:151], v[140:141], off
	v_lshl_add_u64 v[140:141], v[140:141], 0, s[98:99]
	global_load_dwordx4 v[152:155], v[140:141], off
	v_lshl_add_u64 v[140:141], v[140:141], 0, s[98:99]
	global_load_dwordx4 v[156:159], v[140:141], off
	v_lshl_add_u64 v[140:141], v[140:141], 0, s[98:99]
	global_load_dwordx4 v[160:163], v[140:141], off
	v_lshl_add_u64 v[140:141], v[140:141], 0, s[98:99]
	global_load_dwordx4 v[164:167], v[140:141], off
	v_lshl_add_u64 v[140:141], v[140:141], 0, s[98:99]
	global_load_dwordx4 v[168:171], v[140:141], off
	v_lshl_add_u64 v[140:141], v[140:141], 0, s[98:99]
	global_load_dwordx4 v[172:175], v[140:141], off
	v_lshl_add_u64 v[140:141], v[140:141], 0, s[98:99]
	global_load_dwordx4 v[176:179], v[140:141], off
	v_lshl_add_u64 v[140:141], v[140:141], 0, s[98:99]
	global_load_dwordx4 v[180:183], v[140:141], off
	v_lshl_add_u64 v[140:141], v[140:141], 0, s[98:99]
	global_load_dwordx4 v[184:187], v[140:141], off
	v_lshl_add_u64 v[140:141], v[140:141], 0, s[98:99]
	global_load_dwordx4 v[188:191], v[140:141], off
	v_lshl_add_u64 v[140:141], v[140:141], 0, s[98:99]
	global_load_dwordx4 v[192:195], v[140:141], off
	v_lshl_add_u64 v[140:141], v[140:141], 0, s[98:99]
	global_load_dwordx4 v[196:199], v[140:141], off
	v_lshl_add_u64 v[140:141], v[140:141], 0, s[98:99]
	global_load_dwordx4 v[200:203], v[140:141], off
	v_lshl_add_u64 v[140:141], v[140:141], 0, s[98:99]
	global_load_dwordx4 v[204:207], v[140:141], off
	v_lshl_add_u64 v[140:141], v[140:141], 0, s[98:99]
	s_waitcnt vmcnt(15)
	v_bfe_u32 v5, v144, 16, 1
	v_bfe_u32 v10, v145, 16, 1
	v_bfe_u32 v11, v146, 16, 1
	v_bfe_u32 v12, v147, 16, 1
	v_add3_u32 v5, v144, v5, s3
	v_add3_u32 v6, v145, v10, s3
	v_add3_u32 v7, v146, v11, s3
	v_add3_u32 v12, v147, v12, s3
	v_lshrrev_b32_e32 v5, 16, v5
	v_lshrrev_b32_e32 v7, 16, v7
	v_and_or_b32 v6, v6, s18, v5
	v_and_or_b32 v7, v12, s18, v7
	ds_write_b64 v3, v[6:7]
	s_waitcnt vmcnt(14)
	v_bfe_u32 v5, v148, 16, 1
	v_bfe_u32 v10, v149, 16, 1
	v_bfe_u32 v11, v150, 16, 1
	v_bfe_u32 v12, v151, 16, 1
	v_add3_u32 v5, v148, v5, s3
	v_add3_u32 v6, v149, v10, s3
	v_add3_u32 v7, v150, v11, s3
	v_add3_u32 v12, v151, v12, s3
	v_lshrrev_b32_e32 v5, 16, v5
	v_lshrrev_b32_e32 v7, 16, v7
	v_and_or_b32 v6, v6, s18, v5
	v_and_or_b32 v7, v12, s18, v7
	ds_write_b64 v3, v[6:7] offset:4096
	s_waitcnt vmcnt(13)
	v_bfe_u32 v5, v152, 16, 1
	v_bfe_u32 v10, v153, 16, 1
	v_bfe_u32 v11, v154, 16, 1
	v_bfe_u32 v12, v155, 16, 1
	v_add3_u32 v5, v152, v5, s3
	v_add3_u32 v6, v153, v10, s3
	v_add3_u32 v7, v154, v11, s3
	v_add3_u32 v12, v155, v12, s3
	v_lshrrev_b32_e32 v5, 16, v5
	v_lshrrev_b32_e32 v7, 16, v7
	v_and_or_b32 v6, v6, s18, v5
	v_and_or_b32 v7, v12, s18, v7
	ds_write_b64 v3, v[6:7] offset:8192
	s_waitcnt vmcnt(12)
	v_bfe_u32 v5, v156, 16, 1
	v_bfe_u32 v10, v157, 16, 1
	v_bfe_u32 v11, v158, 16, 1
	v_bfe_u32 v12, v159, 16, 1
	v_add3_u32 v5, v156, v5, s3
	v_add3_u32 v6, v157, v10, s3
	v_add3_u32 v7, v158, v11, s3
	v_add3_u32 v12, v159, v12, s3
	v_lshrrev_b32_e32 v5, 16, v5
	v_lshrrev_b32_e32 v7, 16, v7
	v_and_or_b32 v6, v6, s18, v5
	v_and_or_b32 v7, v12, s18, v7
	ds_write_b64 v3, v[6:7] offset:12288
	s_waitcnt vmcnt(11)
	v_bfe_u32 v5, v160, 16, 1
	v_bfe_u32 v10, v161, 16, 1
	v_bfe_u32 v11, v162, 16, 1
	v_bfe_u32 v12, v163, 16, 1
	v_add3_u32 v5, v160, v5, s3
	v_add3_u32 v6, v161, v10, s3
	v_add3_u32 v7, v162, v11, s3
	v_add3_u32 v12, v163, v12, s3
	v_lshrrev_b32_e32 v5, 16, v5
	v_lshrrev_b32_e32 v7, 16, v7
	v_and_or_b32 v6, v6, s18, v5
	v_and_or_b32 v7, v12, s18, v7
	ds_write_b64 v3, v[6:7] offset:16384
	s_waitcnt vmcnt(10)
	v_bfe_u32 v5, v164, 16, 1
	v_bfe_u32 v10, v165, 16, 1
	v_bfe_u32 v11, v166, 16, 1
	v_bfe_u32 v12, v167, 16, 1
	v_add3_u32 v5, v164, v5, s3
	v_add3_u32 v6, v165, v10, s3
	v_add3_u32 v7, v166, v11, s3
	v_add3_u32 v12, v167, v12, s3
	v_lshrrev_b32_e32 v5, 16, v5
	v_lshrrev_b32_e32 v7, 16, v7
	v_and_or_b32 v6, v6, s18, v5
	v_and_or_b32 v7, v12, s18, v7
	ds_write_b64 v3, v[6:7] offset:20480
	s_waitcnt vmcnt(9)
	v_bfe_u32 v5, v168, 16, 1
	v_bfe_u32 v10, v169, 16, 1
	v_bfe_u32 v11, v170, 16, 1
	v_bfe_u32 v12, v171, 16, 1
	v_add3_u32 v5, v168, v5, s3
	v_add3_u32 v6, v169, v10, s3
	v_add3_u32 v7, v170, v11, s3
	v_add3_u32 v12, v171, v12, s3
	v_lshrrev_b32_e32 v5, 16, v5
	v_lshrrev_b32_e32 v7, 16, v7
	v_and_or_b32 v6, v6, s18, v5
	v_and_or_b32 v7, v12, s18, v7
	ds_write_b64 v3, v[6:7] offset:24576
	s_waitcnt vmcnt(8)
	v_bfe_u32 v5, v172, 16, 1
	v_bfe_u32 v10, v173, 16, 1
	v_bfe_u32 v11, v174, 16, 1
	v_bfe_u32 v12, v175, 16, 1
	v_add3_u32 v5, v172, v5, s3
	v_add3_u32 v6, v173, v10, s3
	v_add3_u32 v7, v174, v11, s3
	v_add3_u32 v12, v175, v12, s3
	v_lshrrev_b32_e32 v5, 16, v5
	v_lshrrev_b32_e32 v7, 16, v7
	v_and_or_b32 v6, v6, s18, v5
	v_and_or_b32 v7, v12, s18, v7
	ds_write_b64 v3, v[6:7] offset:28672
	s_waitcnt vmcnt(7)
	v_bfe_u32 v5, v176, 16, 1
	v_bfe_u32 v10, v177, 16, 1
	v_bfe_u32 v11, v178, 16, 1
	v_bfe_u32 v12, v179, 16, 1
	v_add3_u32 v5, v176, v5, s3
	v_add3_u32 v6, v177, v10, s3
	v_add3_u32 v7, v178, v11, s3
	v_add3_u32 v12, v179, v12, s3
	v_lshrrev_b32_e32 v5, 16, v5
	v_lshrrev_b32_e32 v7, 16, v7
	v_and_or_b32 v6, v6, s18, v5
	v_and_or_b32 v7, v12, s18, v7
	ds_write_b64 v3, v[6:7] offset:32768
	s_waitcnt vmcnt(6)
	v_bfe_u32 v5, v180, 16, 1
	v_bfe_u32 v10, v181, 16, 1
	v_bfe_u32 v11, v182, 16, 1
	v_bfe_u32 v12, v183, 16, 1
	v_add3_u32 v5, v180, v5, s3
	v_add3_u32 v6, v181, v10, s3
	v_add3_u32 v7, v182, v11, s3
	v_add3_u32 v12, v183, v12, s3
	v_lshrrev_b32_e32 v5, 16, v5
	v_lshrrev_b32_e32 v7, 16, v7
	v_and_or_b32 v6, v6, s18, v5
	v_and_or_b32 v7, v12, s18, v7
	ds_write_b64 v3, v[6:7] offset:36864
	s_waitcnt vmcnt(5)
	v_bfe_u32 v5, v184, 16, 1
	v_bfe_u32 v10, v185, 16, 1
	v_bfe_u32 v11, v186, 16, 1
	v_bfe_u32 v12, v187, 16, 1
	v_add3_u32 v5, v184, v5, s3
	v_add3_u32 v6, v185, v10, s3
	v_add3_u32 v7, v186, v11, s3
	v_add3_u32 v12, v187, v12, s3
	v_lshrrev_b32_e32 v5, 16, v5
	v_lshrrev_b32_e32 v7, 16, v7
	v_and_or_b32 v6, v6, s18, v5
	v_and_or_b32 v7, v12, s18, v7
	ds_write_b64 v3, v[6:7] offset:40960
	s_waitcnt vmcnt(4)
	v_bfe_u32 v5, v188, 16, 1
	v_bfe_u32 v10, v189, 16, 1
	v_bfe_u32 v11, v190, 16, 1
	v_bfe_u32 v12, v191, 16, 1
	v_add3_u32 v5, v188, v5, s3
	v_add3_u32 v6, v189, v10, s3
	v_add3_u32 v7, v190, v11, s3
	v_add3_u32 v12, v191, v12, s3
	v_lshrrev_b32_e32 v5, 16, v5
	v_lshrrev_b32_e32 v7, 16, v7
	v_and_or_b32 v6, v6, s18, v5
	v_and_or_b32 v7, v12, s18, v7
	ds_write_b64 v3, v[6:7] offset:45056
	s_waitcnt vmcnt(3)
	v_bfe_u32 v5, v192, 16, 1
	v_bfe_u32 v10, v193, 16, 1
	v_bfe_u32 v11, v194, 16, 1
	v_bfe_u32 v12, v195, 16, 1
	v_add3_u32 v5, v192, v5, s3
	v_add3_u32 v6, v193, v10, s3
	v_add3_u32 v7, v194, v11, s3
	v_add3_u32 v12, v195, v12, s3
	v_lshrrev_b32_e32 v5, 16, v5
	v_lshrrev_b32_e32 v7, 16, v7
	v_and_or_b32 v6, v6, s18, v5
	v_and_or_b32 v7, v12, s18, v7
	ds_write_b64 v3, v[6:7] offset:49152
	s_waitcnt vmcnt(2)
	v_bfe_u32 v5, v196, 16, 1
	v_bfe_u32 v10, v197, 16, 1
	v_bfe_u32 v11, v198, 16, 1
	v_bfe_u32 v12, v199, 16, 1
	v_add3_u32 v5, v196, v5, s3
	v_add3_u32 v6, v197, v10, s3
	v_add3_u32 v7, v198, v11, s3
	v_add3_u32 v12, v199, v12, s3
	v_lshrrev_b32_e32 v5, 16, v5
	v_lshrrev_b32_e32 v7, 16, v7
	v_and_or_b32 v6, v6, s18, v5
	v_and_or_b32 v7, v12, s18, v7
	ds_write_b64 v3, v[6:7] offset:53248
	s_waitcnt vmcnt(1)
	v_bfe_u32 v5, v200, 16, 1
	v_bfe_u32 v10, v201, 16, 1
	v_bfe_u32 v11, v202, 16, 1
	v_bfe_u32 v12, v203, 16, 1
	v_add3_u32 v5, v200, v5, s3
	v_add3_u32 v6, v201, v10, s3
	v_add3_u32 v7, v202, v11, s3
	v_add3_u32 v12, v203, v12, s3
	v_lshrrev_b32_e32 v5, 16, v5
	v_lshrrev_b32_e32 v7, 16, v7
	v_and_or_b32 v6, v6, s18, v5
	v_and_or_b32 v7, v12, s18, v7
	ds_write_b64 v3, v[6:7] offset:57344
	s_waitcnt vmcnt(0)
	v_bfe_u32 v5, v204, 16, 1
	v_bfe_u32 v10, v205, 16, 1
	v_bfe_u32 v11, v206, 16, 1
	v_bfe_u32 v12, v207, 16, 1
	v_add3_u32 v5, v204, v5, s3
	v_add3_u32 v6, v205, v10, s3
	v_add3_u32 v7, v206, v11, s3
	v_add3_u32 v12, v207, v12, s3
	v_lshrrev_b32_e32 v5, 16, v5
	v_lshrrev_b32_e32 v7, 16, v7
	v_and_or_b32 v6, v6, s18, v5
	v_and_or_b32 v7, v12, s18, v7
	ds_write_b64 v3, v[6:7] offset:61440

.LBB0_1805:
	v_ashrrev_i32_e32 v12, 5, v6
	v_ashrrev_i32_e32 v13, 31, v12
	v_lshl_add_u64 v[8:9], v[12:13], 0, s[14:15]
	v_lshlrev_b64 v[8:9], 9, v[8:9]
	v_lshl_add_u64 v[150:151], v[2:3], 0, v[8:9]
	v_mad_u64_u32 v[12:13], s[24:25], v12, s21, v[4:5]
	s_mov_b64 s[98:99], 0x2000
	global_load_dwordx4 v[86:89], v[150:151], off
	v_lshl_add_u64 v[150:151], v[150:151], 0, s[98:99]
	global_load_dwordx4 v[90:93], v[150:151], off
	v_lshl_add_u64 v[150:151], v[150:151], 0, s[98:99]
	global_load_dwordx4 v[94:97], v[150:151], off
	v_lshl_add_u64 v[150:151], v[150:151], 0, s[98:99]
	global_load_dwordx4 v[98:101], v[150:151], off
	v_lshl_add_u64 v[150:151], v[150:151], 0, s[98:99]
	global_load_dwordx4 v[102:105], v[150:151], off
	v_lshl_add_u64 v[150:151], v[150:151], 0, s[98:99]
	global_load_dwordx4 v[106:109], v[150:151], off
	v_lshl_add_u64 v[150:151], v[150:151], 0, s[98:99]
	global_load_dwordx4 v[110:113], v[150:151], off
	v_lshl_add_u64 v[150:151], v[150:151], 0, s[98:99]
	global_load_dwordx4 v[114:117], v[150:151], off
	v_lshl_add_u64 v[150:151], v[150:151], 0, s[98:99]
	global_load_dwordx4 v[118:121], v[150:151], off
	v_lshl_add_u64 v[150:151], v[150:151], 0, s[98:99]
	global_load_dwordx4 v[122:125], v[150:151], off
	v_lshl_add_u64 v[150:151], v[150:151], 0, s[98:99]
	global_load_dwordx4 v[126:129], v[150:151], off
	v_lshl_add_u64 v[150:151], v[150:151], 0, s[98:99]
	global_load_dwordx4 v[130:133], v[150:151], off
	v_lshl_add_u64 v[150:151], v[150:151], 0, s[98:99]
	global_load_dwordx4 v[134:137], v[150:151], off
	v_lshl_add_u64 v[150:151], v[150:151], 0, s[98:99]
	global_load_dwordx4 v[138:141], v[150:151], off
	v_lshl_add_u64 v[150:151], v[150:151], 0, s[98:99]
	global_load_dwordx4 v[142:145], v[150:151], off
	v_lshl_add_u64 v[150:151], v[150:151], 0, s[98:99]
	global_load_dwordx4 v[146:149], v[150:151], off
	v_lshl_add_u64 v[150:151], v[150:151], 0, s[98:99]
	s_waitcnt vmcnt(15)
	v_bfe_u32 v7, v86, 16, 1
	v_bfe_u32 v13, v87, 16, 1
	v_bfe_u32 v14, v88, 16, 1
	v_bfe_u32 v15, v89, 16, 1
	v_add3_u32 v7, v86, v7, s19
	v_add3_u32 v8, v87, v13, s19
	v_add3_u32 v9, v88, v14, s19
	v_add3_u32 v15, v89, v15, s19
	v_lshrrev_b32_e32 v7, 16, v7
	v_lshrrev_b32_e32 v9, 16, v9
	v_and_or_b32 v8, v8, s20, v7
	v_and_or_b32 v9, v15, s20, v9
	ds_write_b64 v12, v[8:9]
	s_waitcnt vmcnt(14)
	v_bfe_u32 v7, v90, 16, 1
	v_bfe_u32 v13, v91, 16, 1
	v_bfe_u32 v14, v92, 16, 1
	v_bfe_u32 v15, v93, 16, 1
	v_add3_u32 v7, v90, v7, s19
	v_add3_u32 v8, v91, v13, s19
	v_add3_u32 v9, v92, v14, s19
	v_add3_u32 v15, v93, v15, s19
	v_lshrrev_b32_e32 v7, 16, v7
	v_lshrrev_b32_e32 v9, 16, v9
	v_and_or_b32 v8, v8, s20, v7
	v_and_or_b32 v9, v15, s20, v9
	ds_write_b64 v12, v[8:9] offset:4352
	s_waitcnt vmcnt(13)
	v_bfe_u32 v7, v94, 16, 1
	v_bfe_u32 v13, v95, 16, 1
	v_bfe_u32 v14, v96, 16, 1
	v_bfe_u32 v15, v97, 16, 1
	v_add3_u32 v7, v94, v7, s19
	v_add3_u32 v8, v95, v13, s19
	v_add3_u32 v9, v96, v14, s19
	v_add3_u32 v15, v97, v15, s19
	v_lshrrev_b32_e32 v7, 16, v7
	v_lshrrev_b32_e32 v9, 16, v9
	v_and_or_b32 v8, v8, s20, v7
	v_and_or_b32 v9, v15, s20, v9
	ds_write_b64 v12, v[8:9] offset:8704
	s_waitcnt vmcnt(12)
	v_bfe_u32 v7, v98, 16, 1
	v_bfe_u32 v13, v99, 16, 1
	v_bfe_u32 v14, v100, 16, 1
	v_bfe_u32 v15, v101, 16, 1
	v_add3_u32 v7, v98, v7, s19
	v_add3_u32 v8, v99, v13, s19
	v_add3_u32 v9, v100, v14, s19
	v_add3_u32 v15, v101, v15, s19
	v_lshrrev_b32_e32 v7, 16, v7
	v_lshrrev_b32_e32 v9, 16, v9
	v_and_or_b32 v8, v8, s20, v7
	v_and_or_b32 v9, v15, s20, v9
	ds_write_b64 v12, v[8:9] offset:13056
	s_waitcnt vmcnt(11)
	v_bfe_u32 v7, v102, 16, 1
	v_bfe_u32 v13, v103, 16, 1
	v_bfe_u32 v14, v104, 16, 1
	v_bfe_u32 v15, v105, 16, 1
	v_add3_u32 v7, v102, v7, s19
	v_add3_u32 v8, v103, v13, s19
	v_add3_u32 v9, v104, v14, s19
	v_add3_u32 v15, v105, v15, s19
	v_lshrrev_b32_e32 v7, 16, v7
	v_lshrrev_b32_e32 v9, 16, v9
	v_and_or_b32 v8, v8, s20, v7
	v_and_or_b32 v9, v15, s20, v9
	ds_write_b64 v12, v[8:9] offset:17408
	s_waitcnt vmcnt(10)
	v_bfe_u32 v7, v106, 16, 1
	v_bfe_u32 v13, v107, 16, 1
	v_bfe_u32 v14, v108, 16, 1
	v_bfe_u32 v15, v109, 16, 1
	v_add3_u32 v7, v106, v7, s19
	v_add3_u32 v8, v107, v13, s19
	v_add3_u32 v9, v108, v14, s19
	v_add3_u32 v15, v109, v15, s19
	v_lshrrev_b32_e32 v7, 16, v7
	v_lshrrev_b32_e32 v9, 16, v9
	v_and_or_b32 v8, v8, s20, v7
	v_and_or_b32 v9, v15, s20, v9
	ds_write_b64 v12, v[8:9] offset:21760
	s_waitcnt vmcnt(9)
	v_bfe_u32 v7, v110, 16, 1
	v_bfe_u32 v13, v111, 16, 1
	v_bfe_u32 v14, v112, 16, 1
	v_bfe_u32 v15, v113, 16, 1
	v_add3_u32 v7, v110, v7, s19
	v_add3_u32 v8, v111, v13, s19
	v_add3_u32 v9, v112, v14, s19
	v_add3_u32 v15, v113, v15, s19
	v_lshrrev_b32_e32 v7, 16, v7
	v_lshrrev_b32_e32 v9, 16, v9
	v_and_or_b32 v8, v8, s20, v7
	v_and_or_b32 v9, v15, s20, v9
	ds_write_b64 v12, v[8:9] offset:26112
	s_waitcnt vmcnt(8)
	v_bfe_u32 v7, v114, 16, 1
	v_bfe_u32 v13, v115, 16, 1
	v_bfe_u32 v14, v116, 16, 1
	v_bfe_u32 v15, v117, 16, 1
	v_add3_u32 v7, v114, v7, s19
	v_add3_u32 v8, v115, v13, s19
	v_add3_u32 v9, v116, v14, s19
	v_add3_u32 v15, v117, v15, s19
	v_lshrrev_b32_e32 v7, 16, v7
	v_lshrrev_b32_e32 v9, 16, v9
	v_and_or_b32 v8, v8, s20, v7
	v_and_or_b32 v9, v15, s20, v9
	ds_write_b64 v12, v[8:9] offset:30464
	s_waitcnt vmcnt(7)
	v_bfe_u32 v7, v118, 16, 1
	v_bfe_u32 v13, v119, 16, 1
	v_bfe_u32 v14, v120, 16, 1
	v_bfe_u32 v15, v121, 16, 1
	v_add3_u32 v7, v118, v7, s19
	v_add3_u32 v8, v119, v13, s19
	v_add3_u32 v9, v120, v14, s19
	v_add3_u32 v15, v121, v15, s19
	v_lshrrev_b32_e32 v7, 16, v7
	v_lshrrev_b32_e32 v9, 16, v9
	v_and_or_b32 v8, v8, s20, v7
	v_and_or_b32 v9, v15, s20, v9
	ds_write_b64 v12, v[8:9] offset:34816
	s_waitcnt vmcnt(6)
	v_bfe_u32 v7, v122, 16, 1
	v_bfe_u32 v13, v123, 16, 1
	v_bfe_u32 v14, v124, 16, 1
	v_bfe_u32 v15, v125, 16, 1
	v_add3_u32 v7, v122, v7, s19
	v_add3_u32 v8, v123, v13, s19
	v_add3_u32 v9, v124, v14, s19
	v_add3_u32 v15, v125, v15, s19
	v_lshrrev_b32_e32 v7, 16, v7
	v_lshrrev_b32_e32 v9, 16, v9
	v_and_or_b32 v8, v8, s20, v7
	v_and_or_b32 v9, v15, s20, v9
	ds_write_b64 v12, v[8:9] offset:39168
	s_waitcnt vmcnt(5)
	v_bfe_u32 v7, v126, 16, 1
	v_bfe_u32 v13, v127, 16, 1
	v_bfe_u32 v14, v128, 16, 1
	v_bfe_u32 v15, v129, 16, 1
	v_add3_u32 v7, v126, v7, s19
	v_add3_u32 v8, v127, v13, s19
	v_add3_u32 v9, v128, v14, s19
	v_add3_u32 v15, v129, v15, s19
	v_lshrrev_b32_e32 v7, 16, v7
	v_lshrrev_b32_e32 v9, 16, v9
	v_and_or_b32 v8, v8, s20, v7
	v_and_or_b32 v9, v15, s20, v9
	ds_write_b64 v12, v[8:9] offset:43520
	s_waitcnt vmcnt(4)
	v_bfe_u32 v7, v130, 16, 1
	v_bfe_u32 v13, v131, 16, 1
	v_bfe_u32 v14, v132, 16, 1
	v_bfe_u32 v15, v133, 16, 1
	v_add3_u32 v7, v130, v7, s19
	v_add3_u32 v8, v131, v13, s19
	v_add3_u32 v9, v132, v14, s19
	v_add3_u32 v15, v133, v15, s19
	v_lshrrev_b32_e32 v7, 16, v7
	v_lshrrev_b32_e32 v9, 16, v9
	v_and_or_b32 v8, v8, s20, v7
	v_and_or_b32 v9, v15, s20, v9
	ds_write_b64 v12, v[8:9] offset:47872
	s_waitcnt vmcnt(3)
	v_bfe_u32 v7, v134, 16, 1
	v_bfe_u32 v13, v135, 16, 1
	v_bfe_u32 v14, v136, 16, 1
	v_bfe_u32 v15, v137, 16, 1
	v_add3_u32 v7, v134, v7, s19
	v_add3_u32 v8, v135, v13, s19
	v_add3_u32 v9, v136, v14, s19
	v_add3_u32 v15, v137, v15, s19
	v_lshrrev_b32_e32 v7, 16, v7
	v_lshrrev_b32_e32 v9, 16, v9
	v_and_or_b32 v8, v8, s20, v7
	v_and_or_b32 v9, v15, s20, v9
	ds_write_b64 v12, v[8:9] offset:52224
	s_waitcnt vmcnt(2)
	v_bfe_u32 v7, v138, 16, 1
	v_bfe_u32 v13, v139, 16, 1
	v_bfe_u32 v14, v140, 16, 1
	v_bfe_u32 v15, v141, 16, 1
	v_add3_u32 v7, v138, v7, s19
	v_add3_u32 v8, v139, v13, s19
	v_add3_u32 v9, v140, v14, s19
	v_add3_u32 v15, v141, v15, s19
	v_lshrrev_b32_e32 v7, 16, v7
	v_lshrrev_b32_e32 v9, 16, v9
	v_and_or_b32 v8, v8, s20, v7
	v_and_or_b32 v9, v15, s20, v9
	ds_write_b64 v12, v[8:9] offset:56576
	s_waitcnt vmcnt(1)
	v_bfe_u32 v7, v142, 16, 1
	v_bfe_u32 v13, v143, 16, 1
	v_bfe_u32 v14, v144, 16, 1
	v_bfe_u32 v15, v145, 16, 1
	v_add3_u32 v7, v142, v7, s19
	v_add3_u32 v8, v143, v13, s19
	v_add3_u32 v9, v144, v14, s19
	v_add3_u32 v15, v145, v15, s19
	v_lshrrev_b32_e32 v7, 16, v7
	v_lshrrev_b32_e32 v9, 16, v9
	v_and_or_b32 v8, v8, s20, v7
	v_and_or_b32 v9, v15, s20, v9
	ds_write_b64 v12, v[8:9] offset:60928
	s_waitcnt vmcnt(0)
	v_bfe_u32 v7, v146, 16, 1
	v_bfe_u32 v13, v147, 16, 1
	v_bfe_u32 v14, v148, 16, 1
	v_bfe_u32 v15, v149, 16, 1
	v_add3_u32 v7, v146, v7, s19
	v_add3_u32 v8, v147, v13, s19
	v_add3_u32 v9, v148, v14, s19
	v_add3_u32 v15, v149, v15, s19
	v_lshrrev_b32_e32 v7, 16, v7
	v_lshrrev_b32_e32 v9, 16, v9
	v_and_or_b32 v8, v8, s20, v7
	v_and_or_b32 v9, v15, s20, v9
	ds_write_b64 v12, v[8:9] offset:65280
